# speedup vs baseline: 1.0200x; 1.0153x over previous
.LBB0_33:
	s_waitcnt vmcnt(15)
	v_lshl_add_u64 v[34:35], v[46:47], 2, s[48:49]
	v_add_co_u32_e32 v36, vcc, 0x2000, v34
	v_lshlrev_b32_e32 v1, 2, v231
	s_nop 0
	v_addc_co_u32_e32 v37, vcc, 0, v35, vcc
	s_waitcnt lgkmcnt(0)
	global_load_dword v104, v1, s[60:61]
	global_load_dword v100, v1, s[62:63]
	global_load_dwordx4 v[38:41], v[34:35], off
	s_nop 0
	global_load_dwordx4 v[34:37], v[36:37], off
	v_bfe_u32 v0, v0, 6, 2
	s_waitcnt vmcnt(17)
	v_and_b32_e32 v42, 6, v222
	v_lshl_or_b32 v0, v214, 4, v0
	v_mov_b32_e32 v43, 0x10000
	s_waitcnt vmcnt(15)
	v_lshl_or_b32 v103, v220, 3, v43
	v_lshlrev_b32_e32 v42, 1, v42
	v_mul_u32_u24_e32 v0, 0x110, v0
	v_cvt_pk_f16_f32 v2, v18, v2
	v_add3_u32 v18, v103, v42, v0
	v_cvt_pk_f16_f32 v0, v22, v6
	ds_write2st64_b32 v18, v2, v0 offset1:34
	v_cvt_pk_f16_f32 v2, v26, v10
	v_cvt_pk_f16_f32 v0, v30, v14
	ds_write2st64_b32 v18, v2, v0 offset0:68 offset1:102
	v_add_u32_e32 v6, 0x440, v18
	v_cvt_pk_f16_f32 v2, v19, v3
	v_cvt_pk_f16_f32 v0, v23, v7
	ds_write2st64_b32 v6, v2, v0 offset1:34
	v_cvt_pk_f16_f32 v2, v27, v11
	v_cvt_pk_f16_f32 v0, v31, v15
	ds_write2st64_b32 v6, v2, v0 offset0:68 offset1:102
	v_add_u32_e32 v6, 0x880, v18
	v_cvt_pk_f16_f32 v2, v20, v4
	v_cvt_pk_f16_f32 v0, v24, v8
	ds_write2st64_b32 v6, v2, v0 offset1:34
	v_cvt_pk_f16_f32 v2, v28, v12
	v_cvt_pk_f16_f32 v0, v32, v16
	ds_write2st64_b32 v6, v2, v0 offset0:68 offset1:102
	v_add_u32_e32 v6, 0xcc0, v18
	v_cvt_pk_f16_f32 v2, v21, v5
	v_cvt_pk_f16_f32 v0, v25, v9
	ds_write2st64_b32 v6, v2, v0 offset1:34
	v_cvt_pk_f16_f32 v2, v29, v13
	v_cvt_pk_f16_f32 v0, v33, v17
	ds_write2st64_b32 v6, v2, v0 offset0:68 offset1:102
	v_mbcnt_lo_u32_b32 v0, -1, 0
	v_mbcnt_hi_u32_b32 v101, -1, v0
	v_and_b32_e32 v2, 64, v101
	v_xor_b32_e32 v0, 32, v101
	v_add_u32_e32 v2, 64, v2
	v_cmp_lt_i32_e32 vcc, v0, v2
	s_load_dword s10, s[66:67], 0x0
	v_cndmask_b32_e32 v0, v101, v0, vcc
	v_lshlrev_b32_e32 v102, 2, v0
	ds_bpermute_b32 v0, v102, v217
	v_cmp_gt_u32_e32 vcc, 32, v218
	v_lshlrev_b32_e32 v1, 2, v220
	s_movk_i32 s6, 0x110
	s_nop 1
	s_and_b64 s[12:13], s[4:5], vcc
	s_and_saveexec_b64 s[0:1], s[12:13]
	s_cbranch_execz .LBB0_35
	s_waitcnt lgkmcnt(0)
	v_add_f32_e32 v0, v217, v0
	v_cvt_f16_f32_e32 v0, v0
	v_lshlrev_b32_e32 v2, 1, v1
	v_lshlrev_b32_e32 v3, 1, v219
	s_mov_b32 s7, 0x21000
	v_add3_u32 v2, v3, v2, s7
	ds_write_b16 v2, v0
